# Y phase: static s_setprio 1 for the weight-conversion waves (4-7), which are the phase's critical path beside the latency-bound scan waves; reset at the phase end
# baseline (speedup 1.0000x reference)
; #define SEAM(k) do { if (IN(k) && IN((k) + 1)) GRID_BAR(); } while (0)
; template <int GRP>
; __device__ __forceinline__ void y_phase(Frame& F, const MW& W) {
;     ...
;         if (F.tid >= 256) {
;             if (base == (int)blockIdx.x * 256 && F.G == 256) {
; #pragma unroll 1
;                 for (int k = 0; k < YK; ++k) conv_item<GRP>(F, (int)blockIdx.x * 4 + (F.wave - 4) + k * 1024);
; template <int L>
; __device__ __forceinline__ void layer(Frame& F, const XcdBarrier& bar, float* out, const int lo, const int hi) {
;     ...
;     const mls::MW mw{ws + WS_CC, ws + WS_CP, (float*)(ws + WS_NC), (float*)(ws + WS_NP), (float*)(ws + WS_SC), (float*)(ws + WS_SC + 65536)};
;     const float* km = (const float*)(ws + WS_CTL + KMEAN_OFF + (size_t)L * 131072);
;     const int cls = (blockIdx.x >> 3) & 3; const bool odd = (cls & 1) != 0;
;     if (IN(pb + 1)) {
;         mls::x_setup(F, inptr(F, IN_CONVW) + (size_t)L * 4 * 1024, inptr(F, IN_CONVB) + (size_t)L * 1024);
;         { int u = blockIdx.x; mls::XL xa; if (u < 1024) mls::x_load(xa, F, proj, gates, u);
;           for (; u < 1024; u += F.G) { mls::XL xb; const bool hn = u + F.G < 1024; mls::x_unit(F, proj, gates, mw, u, xa, xb, hn, u + F.G); xa = xb; } }
;         __syncthreads();
;     }
;     SEAM(pb + 1);
;     if (IN(pb + 2)) {
;         constexpr int GRP = (L == 0) ? 2 : 3;
;         mls::y_phase<GRP>(F, mw);
.LBB0_356:
	s_or_b64 exec, exec, s[0:1]
	v_readlane_b32 s100, v255, 9
	s_cmp_lt_u32 s100, 4
	s_cbranch_scc1 .Lyprio_3
	s_setprio 1
.Lyprio_3:
	s_waitcnt lgkmcnt(0)
	s_barrier
.LBB0_357:
	v_readlane_b32 s0, v255, 11
	s_cmp_lt_i32 s0, 5
	v_readlane_b32 s1, v255, 12
	s_cselect_b64 s[8:9], -1, 0
	s_add_u32 s0, s50, 0x38a00000
	s_addc_u32 s1, s51, 0
	v_writelane_b32 v255, s0, 21
	s_nop 1
	v_writelane_b32 v255, s1, 22
	s_add_u32 s0, s50, 0x3aa00000
	s_addc_u32 s1, s51, 0
	v_writelane_b32 v255, s0, 23
	s_nop 1
	v_writelane_b32 v255, s1, 24
	s_add_u32 s0, s50, 0x3ab00000
	s_addc_u32 s1, s51, 0
	v_writelane_b32 v255, s0, 25
	s_add_u32 s64, s50, 0x3ac10000
	s_addc_u32 s65, s51, 0
	v_writelane_b32 v255, s1, 26
	s_bfe_u32 s0, s2, 0x20003
	s_bitcmp0_b32 s2, 3
	v_writelane_b32 v255, s0, 27
	s_cselect_b64 s[0:1], -1, 0
	v_writelane_b32 v255, s0, 28
	s_add_u32 s5, s50, 0x26200000
	s_addc_u32 s33, s51, 0
	v_writelane_b32 v255, s1, 29
	v_writelane_b32 v255, s8, 30
	s_and_b64 s[0:1], s[8:9], s[6:7]
	s_andn2_b64 vcc, exec, s[0:1]
	v_writelane_b32 v255, s9, 31
	s_cbranch_vccz .LBB0_358
	s_getpc_b64 s[98:99]

; #define GRID_BAR() do { if (N_LAUNCHES == 1) xcd_barrier(bar); } while (0)
;     constexpr int N = (GRP == 0) ? CONV_N0 : (GRP == 1) ? CONV_N1 : (GRP == 2) ? CONV_N2 : (GRP == 3) ? CONV_N3 : CONV_N4;
;     for (int it = first + F.gw; it < N; it += F.NGW) conv_item<GRP>(F, it);
; template <int L>
; __device__ __forceinline__ void layer(Frame& F, const XcdBarrier& bar, float* out, const int lo, const int hi) {
;     ...
;         GRID_BAR();
;         if (cls == 0) { conv_all<GRP>(F, (F.G == 256) ? ((L == 0) ? SLOT_FIRST0 : SLOT_FIRST1) : 0); if (L == 0 && F.G == 256) { const int e4 = F.gw - G4_SLACK0; if (e4 >= 0 && e4 < G4_TAIL) conv_item<4>(F, 2048 + e4); } __syncthreads(); }
.LBB0_503:
	s_or_b64 exec, exec, s[0:1]
	s_setprio 0
	v_readlane_b32 s0, v255, 27
	s_cmp_lg_u32 s0, 0
	s_waitcnt lgkmcnt(0)
	s_barrier
	s_cbranch_scc1 .LBB0_527
	s_cmpk_eq_i32 s48, 0x100
	s_cselect_b64 s[0:1], -1, 0
	s_and_b64 s[6:7], s[0:1], exec
	s_cselect_b32 s3, 0x15b0, 0
	v_readlane_b32 s4, v255, 10
	s_add_i32 s3, s3, s4
	s_cmpk_gt_i32 s3, 0x3c2f
	s_cbranch_scc1 .LBB0_524
	v_readlane_b32 s4, v255, 9
	s_mulk_i32 s4, 0x2200
	v_lshrrev_b32_e32 v1, 1, v0
	v_mov_b32_e32 v11, 0
	v_lshlrev_b32_e32 v10, 4, v194
	s_add_i32 s4, s4, 0
	v_and_b32_e32 v15, 28, v1
	v_lshl_add_u64 v[6:7], s[50:51], 0, v[10:11]
	s_mov_b64 s[10:11], 0xbbc00
	v_and_b32_e32 v1, 7, v0
	v_lshl_add_u64 v[12:13], v[6:7], 0, s[10:11]
	s_add_u32 s10, s50, 0x8b000
	v_lshlrev_b32_e32 v14, 2, v1
	v_mul_u32_u24_e32 v23, 0x210, v1
	v_lshlrev_b32_e32 v16, 4, v1
	v_mbcnt_lo_u32_b32 v1, -1, 0
	v_lshlrev_b32_e32 v2, 2, v194
	s_addc_u32 s11, s51, 0
	v_lshrrev_b32_e32 v20, 3, v194
	v_mov_b32_e32 v17, v11
	v_mbcnt_hi_u32_b32 v30, -1, v1
	v_and_b32_e32 v4, 28, v2
	s_add_u32 s12, s50, 0x13200000
	v_lshlrev_b32_e32 v21, 2, v20
	v_lshl_add_u64 v[6:7], s[50:51], 0, v[16:17]
	s_mov_b64 s[14:15], 0x3400000
	v_readlane_b32 s8, v255, 13
	v_and_b32_e32 v1, 64, v30
	s_mov_b32 s9, 0
	v_cmp_gt_u32_e64 s[6:7], 8, v194
	s_addc_u32 s13, s51, 0
	v_add_u32_e32 v22, s4, v21
	v_add_u32_e32 v24, s4, v16
	v_mul_u32_u24_e32 v25, 0x84, v20
	v_or_b32_e32 v26, 8, v20
	v_or_b32_e32 v27, 16, v20
	v_or_b32_e32 v28, 24, v20
	v_lshl_add_u64 v[18:19], v[6:7], 0, s[14:15]
	s_lshl_b32 s4, s3, 5
	s_lshl_b32 s22, s8, 5
	s_add_i32 s23, 0, 0x20240
	s_movk_i32 s24, 0x4c20
	s_movk_i32 s25, 0xa0
	s_movk_i32 s26, 0x2000
	s_movk_i32 s27, 0x5000
	s_mov_b32 s28, 0x8000
	s_mov_b32 s29, 0x58000
	s_mov_b32 s30, 0x5a000
	s_mov_b32 s31, 0x5d000
	s_mov_b32 s34, 0x60000
	s_mov_b32 s35, 0xb0000
	s_mov_b32 s36, 0xb2000
	s_mov_b32 s37, 0xb5000
	s_mov_b32 s38, 0xb8000
	s_mov_b32 s39, 0x108000
	s_mov_b32 s40, 0x10a000
	s_mov_b32 s41, 0x10d000
	s_mov_b32 s42, 0x110000
	v_lshlrev_b32_e32 v29, 2, v2
	s_add_i32 s43, 0, 0x202b0
	s_movk_i32 s44, 0x4000
	s_movk_i32 s45, 0x6000
	s_mov_b32 s46, 0x40000
	s_mov_b32 s47, 0x42000
	s_mov_b32 s49, 0x44000
	s_mov_b32 s52, 0x46000
	s_mov_b32 s53, 0x80000
	s_mov_b32 s54, 0x82000
	s_mov_b32 s55, 0x84000
	s_mov_b32 s56, 0x86000
	s_mov_b32 s57, 0xc0000
	s_mov_b32 s62, 0xc2000
	s_mov_b32 s63, 0xc4000
	s_mov_b32 s66, 0xc6000
	s_mov_b32 s67, 0xc3e00000
	s_add_i32 s68, 0, 0x20248
	s_mov_b64 s[14:15], 0x1000000
	v_lshlrev_b32_e32 v10, 2, v4
	v_xor_b32_e32 v31, 8, v30
	v_add_u32_e32 v32, 64, v1
	v_xor_b32_e32 v33, 16, v30
	s_waitcnt vmcnt(14)
	v_xor_b32_e32 v34, 32, v30
	v_mov_b32_e32 v35, 0x580000
	v_mov_b32_e32 v36, 0x1600
	v_mov_b32_e32 v37, 0x43e00000
	v_readlane_b32 s16, v255, 9
	s_cmp_lt_u32 s16, 4
	s_cbranch_scc1 .Lstg_507
	s_sleep 44

; template <int GRP>
; __device__ __forceinline__ void y_phase(Frame& F, const MW& W) {
;     for (int base = blockIdx.x * 256; base < 32 * 2048; base += F.G * 256) {
;         if (F.tid >= 256) {
;             if (base == (int)blockIdx.x * 256 && F.G == 256) {
; #pragma unroll 1
;                 for (int k = 0; k < YK; ++k) conv_item<GRP>(F, (int)blockIdx.x * 4 + (F.wave - 4) + k * 1024);
;             }
;             continue; }
;         const int bh = base >> 11, g = (base & 2047) + F.tid, e = g >> 4, d8 = (g & 15) * 8;
.Lyprio_12:
	s_waitcnt lgkmcnt(0)
	s_barrier
.LBB0_1540:
	v_readlane_b32 s0, v255, 11
	v_readlane_b32 s1, v255, 12
	s_cmp_lt_i32 s0, 13
	s_cselect_b64 s[0:1], -1, 0
	v_writelane_b32 v255, s0, 37
	s_nop 1
	v_writelane_b32 v255, s1, 38
	s_and_b64 s[0:1], s[0:1], s[6:7]
	s_andn2_b64 vcc, exec, s[0:1]
	s_cbranch_vccnz .LBB0_2036
	s_lshl_b32 s0, s2, 8
	v_writelane_b32 v255, s0, 32
	s_cmp_gt_i32 s0, 0xffff
	s_cbranch_scc1 .LBB0_1617
	s_movk_i32 s1, 0x100
	v_cmp_gt_u32_e64 s[6:7], s1, v0
	s_lshl_b32 s0, s2, 2
	s_waitcnt vmcnt(0)
	v_mov_b32_e32 v133, 0
	v_writelane_b32 v255, s6, 33
	v_lshlrev_b32_e32 v132, 4, v0
	s_cmpk_eq_i32 s48, 0x100
	v_writelane_b32 v255, s7, 34
	v_lshlrev_b32_e32 v1, 3, v0
	v_readlane_b32 s6, v255, 23
	v_readlane_b32 s7, v255, 24
	v_and_b32_e32 v130, 0x78, v1
	v_and_b32_e32 v1, 7, v0
	v_lshl_add_u64 v[136:137], s[6:7], 0, v[132:133]
	s_cselect_b64 s[6:7], -1, 0
	v_writelane_b32 v255, s6, 35
	v_lshrrev_b32_e32 v131, 3, v194
	v_lshlrev_b32_e32 v135, 2, v131
	v_writelane_b32 v255, s7, 36
	v_lshlrev_b32_e32 v138, 4, v1
	v_readlane_b32 s3, v255, 9
	s_mul_i32 s1, s3, 0x2200
	s_add_i32 s1, s1, 0
	s_add_u32 s4, s50, 0x8200000
	s_addc_u32 s49, s51, 0
	s_add_u32 s96, s50, 0x8b000
	s_addc_u32 s97, s51, 0
	v_lshlrev_b32_e32 v2, 2, v1
	s_waitcnt lgkmcnt(3)
	v_add_u32_e32 v3, s1, v135
	s_waitcnt lgkmcnt(2)
	v_mul_u32_u24_e32 v4, 0x210, v1
	v_add_u32_e32 v1, s1, v138
	s_lshl_b32 s1, s48, 8
	v_mul_u32_u24_e32 v5, 0x84, v131
	v_writelane_b32 v255, s1, 39
	v_lshlrev_b32_e32 v134, 2, v0
	s_mov_b32 s17, 0
	v_mov_b32_e32 v139, v133
	v_or_b32_e32 v216, 8, v131
	v_or_b32_e32 v217, 16, v131
	v_or_b32_e32 v218, 24, v131
	s_add_i32 s77, s3, s0
	s_mov_b32 s14, 0xc3e00000
	v_lshlrev_b32_e32 v132, 2, v2
	s_mov_b32 s15, 0x42fe0000
	s_mov_b32 s3, 0xc2fe0000
	s_mov_b32 s6, 0xc0c0500
	v_add_u32_e32 v219, v3, v4
	v_add_u32_e32 v220, v1, v5
	v_mov_b32_e32 v221, 0x43e00000
	v_mov_b32_e32 v224, v133
	v_mov_b32_e32 v225, v133
	v_mov_b32_e32 v226, v133
	v_mov_b32_e32 v227, v133
	v_mov_b32_e32 v222, 0x42fe0000
	v_readlane_b32 s7, v255, 32
	s_branch .LBB0_1544

; #define GRID_BAR() do { if (N_LAUNCHES == 1) xcd_barrier(bar); } while (0)
;     constexpr int N = (GRP == 0) ? CONV_N0 : (GRP == 1) ? CONV_N1 : (GRP == 2) ? CONV_N2 : (GRP == 3) ? CONV_N3 : CONV_N4;
;     for (int it = first + F.gw; it < N; it += F.NGW) conv_item<GRP>(F, it);
; template <int L>
; __device__ __forceinline__ void layer(Frame& F, const XcdBarrier& bar, float* out, const int lo, const int hi) {
;     ...
;         GRID_BAR();
;         if (cls == 0) { conv_all<GRP>(F, (F.G == 256) ? ((L == 0) ? SLOT_FIRST0 : SLOT_FIRST1) : 0); if (L == 0 && F.G == 256) { const int e4 = F.gw - G4_SLACK0; if (e4 >= 0 && e4 < G4_TAIL) conv_item<4>(F, 2048 + e4); } __syncthreads(); }
.LBB0_1669:
	s_or_b64 exec, exec, s[0:1]
	s_setprio 0
	v_readlane_b32 s0, v255, 27
	s_cmp_lg_u32 s0, 0
	s_waitcnt lgkmcnt(0)
	s_barrier
	s_cbranch_scc1 .LBB0_1674
	s_cmpk_eq_i32 s48, 0x100
	s_cselect_b32 s0, 0x1800, 0
	v_readlane_b32 s1, v255, 10
	s_add_i32 s3, s0, s1
	s_cmpk_gt_i32 s3, 0x57ff
	v_readlane_b32 s40, v255, 13
	s_cbranch_scc1 .LBB0_1673
	v_readlane_b32 s0, v255, 9
	s_mulk_i32 s0, 0x2200
	s_add_i32 s0, s0, 0
	v_and_b32_e32 v2, 7, v0
	s_add_u32 s4, s50, 0x8200000
	v_lshrrev_b32_e32 v1, 3, v194
	v_lshlrev_b32_e32 v4, 2, v2
	v_mul_u32_u24_e32 v7, 0x210, v2
	v_lshlrev_b32_e32 v2, 4, v2
	s_addc_u32 s12, s51, 0
	v_lshlrev_b32_e32 v16, 2, v1
	v_add_u32_e32 v8, s0, v2
	v_mul_u32_u24_e32 v9, 0x84, v1
	s_add_u32 s13, s50, 0x8b000
	v_mov_b32_e32 v3, 0
	v_add_u32_e32 v6, s0, v16
	v_add_u32_e32 v22, v8, v9
	s_addc_u32 s14, s51, 0
	v_or_b32_e32 v17, 8, v1
	v_or_b32_e32 v18, 16, v1
	v_or_b32_e32 v19, 24, v1
	s_movk_i32 s15, 0xa0
	v_lshlrev_b32_e32 v4, 2, v4
	v_mov_b32_e32 v5, v3
	s_mov_b32 s16, 0x42fe0000
	s_movk_i32 s17, 0x2000
	s_movk_i32 s18, 0x5000
	s_mov_b32 s19, 0x8000
	s_mov_b32 s20, 0x58000
	s_mov_b32 s21, 0x5a000
	s_mov_b32 s22, 0x5d000
	s_mov_b32 s23, 0x60000
	s_mov_b32 s24, 0xb0000
	s_mov_b32 s25, 0xb2000
	s_mov_b32 s26, 0xb5000
	s_mov_b32 s27, 0xb8000
	s_mov_b32 s28, 0x108000
	s_mov_b32 s29, 0x10a000
	s_mov_b32 s30, 0x10d000
	s_mov_b32 s31, 0x110000
	s_mov_b32 s34, 0xc2fe0000
	v_mov_b32_e32 v20, 0x42fe0000
	s_mov_b32 s35, 0xc0c0500
	v_add_u32_e32 v21, v6, v7
	v_add_u32_e32 v23, 0x420, v22
	v_add_u32_e32 v24, 0x428, v22
	v_add_u32_e32 v25, 0x840, v22
	v_add_u32_e32 v26, 0x848, v22
	v_add_u32_e32 v27, 0xc60, v22
	v_add_u32_e32 v28, 0xc68, v22
	v_readlane_b32 s0, v255, 9
	s_cmp_lt_u32 s0, 4
	s_cbranch_scc1 .Lstg_1672
	s_sleep 44
